# router phase loop: next sub-batch row requested at the top of the iteration (after the current row is unpacked) instead of after the router MFMAs
# baseline (speedup 1.0000x reference)
; __device__ __forceinline__ void phase5(Frame& F, const Args& a) {
;     ...
;             f32x4 v[8]; float s = 0.f;
; #pragma unroll
;             for (int j = 0; j < 8; ++j) { const v2u yw = ynx[j]; v[j] = (f32x4){bflo(yw.x), bfhi(yw.x), bflo(yw.y), bfhi(yw.y)}; s += (v[j].x + v[j].y) + (v[j].z + v[j].w); }
;             float mean = wave_sum(s) * (1.f / D); float s2 = 0.f;
; #pragma unroll
;             for (int j = 0; j < 8; ++j) { v[j] = v[j] - mean; s2 += (v[j].x * v[j].x + v[j].y * v[j].y) + (v[j].z * v[j].z + v[j].w * v[j].w); }
;             float rstd = 1.f / sqrtf(wave_sum(s2) * (1.f / D) + LN_EPS);
;     ...
;         if (sb + 8 < rows_per_wg) {
; #pragma unroll
;             for (int j = 0; j < 8; ++j) ynx[j] = *((const v2u*)(Y1 + (size_t)(m + 8) * D) + lane + 64 * j);
;         }
.LBB0_627:
	s_waitcnt vmcnt(6)
	v_lshlrev_b32_e32 v173, 16, v144
	v_lshlrev_b32_e32 v172, 16, v142
	v_and_b32_e32 v177, 0xffff0000, v144
	v_and_b32_e32 v176, 0xffff0000, v142
	v_lshlrev_b32_e32 v131, 16, v145
	v_lshlrev_b32_e32 v130, 16, v143
	v_and_b32_e32 v133, 0xffff0000, v145
	v_and_b32_e32 v132, 0xffff0000, v143
	v_pk_add_f32 v[134:135], v[172:173], v[176:177]
	v_pk_add_f32 v[136:137], v[130:131], v[132:133]
	s_waitcnt vmcnt(5)
	v_lshlrev_b32_e32 v179, 16, v147
	v_pk_add_f32 v[134:135], v[134:135], v[136:137]
	v_lshlrev_b32_e32 v178, 16, v146
	v_and_b32_e32 v181, 0xffff0000, v147
	v_and_b32_e32 v180, 0xffff0000, v146
	v_add_f32_e32 v134, 0, v134
	v_pk_add_f32 v[136:137], v[178:179], v[180:181]
	v_add_f32_e32 v174, v134, v135
	s_waitcnt vmcnt(4)
	v_lshlrev_b32_e32 v134, 16, v148
	v_and_b32_e32 v135, 0xffff0000, v148
	v_lshlrev_b32_e32 v166, 16, v149
	v_and_b32_e32 v167, 0xffff0000, v149
	s_waitcnt vmcnt(3)
	v_and_b32_e32 v193, 0xffff0000, v150
	v_pk_add_f32 v[136:137], v[136:137], v[136:137] op_sel:[0,1] op_sel_hi:[1,0]
	v_add_f32_e32 v188, v134, v135
	v_add_f32_e32 v184, v166, v167
	v_lshlrev_b32_e32 v175, 16, v150
	v_lshlrev_b32_e32 v189, 16, v151
	v_and_b32_e32 v185, 0xffff0000, v151
	v_mov_b32_e32 v137, v193
	v_pk_add_f32 v[136:137], v[174:175], v[136:137]
	v_pk_add_f32 v[168:169], v[188:189], v[184:185]
	s_waitcnt vmcnt(2)
	v_lshlrev_b32_e32 v171, 16, v153
	v_lshlrev_b32_e32 v170, 16, v152
	v_and_b32_e32 v211, 0xffff0000, v153
	v_and_b32_e32 v210, 0xffff0000, v152
	v_pk_add_f32 v[194:195], v[136:137], v[168:169]
	v_pk_add_f32 v[212:213], v[170:171], v[210:211]
	s_waitcnt vmcnt(1)
	v_lshlrev_b32_e32 v182, 16, v154
	v_and_b32_e32 v183, 0xffff0000, v154
	v_lshlrev_b32_e32 v186, 16, v155
	v_and_b32_e32 v187, 0xffff0000, v155
	s_waitcnt vmcnt(0)
	v_lshlrev_b32_e32 v190, 16, v156
	v_and_b32_e32 v191, 0xffff0000, v156
	v_pk_add_f32 v[194:195], v[194:195], v[194:195] op_sel:[0,1] op_sel_hi:[1,0]
	v_pk_add_f32 v[212:213], v[212:213], v[212:213] op_sel:[0,1] op_sel_hi:[1,0]
	v_add_f32_e32 v168, v182, v183
	v_add_f32_e32 v136, v186, v187
	v_lshlrev_b32_e32 v169, 16, v157
	v_and_b32_e32 v137, 0xffff0000, v157
	s_cmp_ge_i32 s1, s30
	s_cbranch_scc1 .Lp6_nopf
	s_add_i32 s98, s0, s1
	s_ashr_i32 s99, s98, 31
	s_lshl_b64 s[98:99], s[98:99], 12
	v_lshl_add_u64 v[244:245], v[162:163], 0, s[98:99]
	global_load_dwordx2 v[142:143], v[244:245], off
	global_load_dwordx2 v[144:145], v[244:245], off offset:512
	global_load_dwordx2 v[146:147], v[244:245], off offset:1024
	global_load_dwordx2 v[148:149], v[244:245], off offset:1536
	global_load_dwordx2 v[150:151], v[244:245], off offset:2048
	global_load_dwordx2 v[152:153], v[244:245], off offset:2560
	global_load_dwordx2 v[154:155], v[244:245], off offset:3072
	global_load_dwordx2 v[156:157], v[244:245], off offset:3584
.Lp6_nopf:
	v_mov_b32_e32 v195, v190
	v_mov_b32_e32 v213, v191
	v_pk_add_f32 v[194:195], v[194:195], v[212:213]
	v_pk_add_f32 v[212:213], v[168:169], v[136:137]
	s_nop 0
	v_pk_add_f32 v[194:195], v[194:195], v[212:213]
	s_nop 0
	v_add_f32_e32 v136, v194, v195
	s_nop 1
	v_add_f32_dpp v136, v136, v136 quad_perm:[1,0,3,2] row_mask:0xf bank_mask:0xf bound_ctrl:1
	s_nop 1
	v_add_f32_dpp v136, v136, v136 quad_perm:[2,3,0,1] row_mask:0xf bank_mask:0xf bound_ctrl:1
	s_nop 1
	v_add_f32_dpp v136, v136, v136 row_half_mirror row_mask:0xf bank_mask:0xf bound_ctrl:1
	s_nop 1
	v_add_f32_dpp v136, v136, v136 row_mirror row_mask:0xf bank_mask:0xf bound_ctrl:1
	s_nop 0
	v_readlane_b32 s24, v136, 16
	v_readlane_b32 s25, v136, 48
	v_readlane_b32 s18, v136, 0
	v_readlane_b32 s19, v136, 32
	v_mov_b32_e32 v194, s24
	v_mov_b32_e32 v195, s25
	v_pk_add_f32 v[194:195], s[18:19], v[194:195]
	s_nop 0
	v_add_f32_e32 v140, v194, v195
	v_fmac_f32_e32 v132, 0xba000000, v140
	v_fmac_f32_e32 v176, 0xba000000, v140
	v_fmac_f32_e32 v133, 0xba000000, v140
	v_fmac_f32_e32 v177, 0xba000000, v140
	v_fmac_f32_e32 v130, 0xba000000, v140
	v_fmac_f32_e32 v172, 0xba000000, v140
	v_fmac_f32_e32 v131, 0xba000000, v140
	v_fmac_f32_e32 v173, 0xba000000, v140
	v_pk_mul_f32 v[194:195], v[176:177], v[176:177]
	v_pk_mul_f32 v[212:213], v[132:133], v[132:133]
	v_fmac_f32_e32 v180, 0xba000000, v140
	v_fmac_f32_e32 v181, 0xba000000, v140
	v_fmac_f32_e32 v179, 0xba000000, v140
	v_pk_fma_f32 v[194:195], v[172:173], v[172:173], v[194:195]
	v_pk_fma_f32 v[212:213], v[130:131], v[130:131], v[212:213]
	v_fmac_f32_e32 v178, 0xba000000, v140
	v_mov_b32_e32 v224, v179
	v_mov_b32_e32 v225, v181
	v_mov_b32_e32 v179, v180
	v_pk_add_f32 v[194:195], v[194:195], v[212:213]
	v_pk_mul_f32 v[212:213], v[224:225], v[224:225]
	v_pk_mul_f32 v[180:181], v[178:179], v[178:179]
	v_fmac_f32_e32 v134, 0xba000000, v140
	v_pk_mov_b32 v[214:215], v[180:181], v[212:213] op_sel:[1,0]
	v_mov_b32_e32 v181, v213
	v_fmac_f32_e32 v135, 0xba000000, v140
	v_fmac_f32_e32 v166, 0xba000000, v140
	v_mul_f32_e32 v136, v134, v134
	v_pk_add_f32 v[180:181], v[214:215], v[180:181]
	v_fmac_f32_e32 v167, 0xba000000, v140
	v_pk_fma_f32 v[212:213], v[134:135], v[134:135], v[136:137] op_sel_hi:[1,1,0]
	v_mul_f32_e32 v136, v166, v166
	v_pk_add_f32 v[194:195], v[194:195], v[194:195] op_sel_hi:[0,1]
	v_pk_add_f32 v[180:181], v[180:181], v[180:181] op_sel_hi:[0,1]
	v_pk_fma_f32 v[214:215], v[166:167], v[166:167], v[136:137] op_sel_hi:[1,1,0]
	v_fmac_f32_e32 v185, 0xba000000, v140
	v_fmac_f32_e32 v189, 0xba000000, v140
	v_fmac_f32_e32 v193, 0xba000000, v140
	v_fmac_f32_e32 v175, 0xba000000, v140
	v_mul_f32_e32 v212, v175, v175
	v_mul_f32_e32 v214, v193, v193
	v_mul_f32_e32 v180, v189, v189
	v_mul_f32_e32 v194, v185, v185
	v_fmac_f32_e32 v210, 0xba000000, v140
	v_fmac_f32_e32 v211, 0xba000000, v140
; #define LAS __attribute__((address_space(3)))
; __device__ __forceinline__ unsigned pk2(float lo, float hi) { return f2bf(lo) | (f2bf(hi) << 16); }
; __device__ __forceinline__ void phase5(Frame& F, const Args& a) {
;     ...
;             for (int j = 0; j < 8; ++j) { v[j] = v[j] - mean; s2 += (v[j].x * v[j].x + v[j].y * v[j].y) + (v[j].z * v[j].z + v[j].w * v[j].w); }
;             float rstd = 1.f / sqrtf(wave_sum(s2) * (1.f / D) + LN_EPS);
;             v2u xw8[8];
;             s = 0.f;
; #pragma unroll
;             for (int j = 0; j < 8; ++j) { if ((j & 3) == 0) asm volatile("" ::: "memory"); const f32x4 gg = *((const LAS f32x4*)prm + lane + 64 * j), bb = *((const LAS f32x4*)(prm + D) + lane + 64 * j);
;                 v[j] = v[j] * rstd * gg + bb; xw8[j].x = pk2(v[j].x, v[j].y); xw8[j].y = pk2(v[j].z, v[j].w); s += (v[j].x + v[j].y) + (v[j].z + v[j].w); }
;             store_row_b8<8, 512>((unsigned char*)(X1 + (size_t)m * D), lane, xw8);
	v_fmac_f32_e32 v171, 0xba000000, v140
	v_pk_add_f32 v[212:213], v[212:213], v[214:215]
	v_pk_add_f32 v[180:181], v[180:181], v[194:195]
	v_fmac_f32_e32 v170, 0xba000000, v140
	v_mov_b32_e32 v194, v171
	v_mov_b32_e32 v195, v211
	v_mov_b32_e32 v171, v210
	v_pk_add_f32 v[180:181], v[212:213], v[180:181]
	v_pk_mul_f32 v[212:213], v[194:195], v[194:195]
	v_pk_mul_f32 v[210:211], v[170:171], v[170:171]
	v_fmac_f32_e32 v182, 0xba000000, v140
	v_pk_mov_b32 v[214:215], v[210:211], v[212:213] op_sel:[1,0]
	v_mov_b32_e32 v211, v213
	v_fmac_f32_e32 v183, 0xba000000, v140
	v_fmac_f32_e32 v186, 0xba000000, v140
	v_mul_f32_e32 v136, v182, v182
	v_pk_add_f32 v[210:211], v[214:215], v[210:211]
	v_fmac_f32_e32 v187, 0xba000000, v140
	v_pk_fma_f32 v[212:213], v[182:183], v[182:183], v[136:137] op_sel_hi:[1,1,0]
	v_mul_f32_e32 v136, v186, v186
	v_pk_add_f32 v[180:181], v[180:181], v[180:181] op_sel_hi:[0,1]
	v_pk_add_f32 v[210:211], v[210:211], v[210:211] op_sel_hi:[0,1]
	v_pk_fma_f32 v[214:215], v[186:187], v[186:187], v[136:137] op_sel_hi:[1,1,0]
	v_fmac_f32_e32 v137, 0xba000000, v140
	v_fmac_f32_e32 v169, 0xba000000, v140
	v_fmac_f32_e32 v191, 0xba000000, v140
	v_fmac_f32_e32 v190, 0xba000000, v140
	v_mul_f32_e32 v212, v190, v190
	v_mul_f32_e32 v214, v191, v191
	v_mul_f32_e32 v210, v169, v169
	v_mul_f32_e32 v180, v137, v137
	v_pk_add_f32 v[212:213], v[212:213], v[214:215]
	v_pk_add_f32 v[180:181], v[210:211], v[180:181]
	v_mov_b32_e32 v222, v173
	v_pk_add_f32 v[180:181], v[212:213], v[180:181]
	v_mov_b32_e32 v173, v176
	v_add_f32_e32 v136, v180, v181
	v_mov_b32_e32 v176, v130
	v_mov_b32_e32 v223, v177
	v_add_f32_dpp v136, v136, v136 quad_perm:[1,0,3,2] row_mask:0xf bank_mask:0xf bound_ctrl:1
	v_mov_b32_e32 v177, v132
	v_mov_b32_e32 v192, v175
	v_add_f32_dpp v136, v136, v136 quad_perm:[2,3,0,1] row_mask:0xf bank_mask:0xf bound_ctrl:1
	v_mov_b32_e32 v184, v189
	s_nop 0
	v_add_f32_dpp v136, v136, v136 row_half_mirror row_mask:0xf bank_mask:0xf bound_ctrl:1
	s_nop 1
	v_add_f32_dpp v136, v136, v136 row_mirror row_mask:0xf bank_mask:0xf bound_ctrl:1
	s_nop 0
	v_readlane_b32 s24, v136, 16
	v_readlane_b32 s25, v136, 48
	v_readlane_b32 s18, v136, 0
	v_readlane_b32 s19, v136, 32
	v_mov_b32_e32 v180, s24
	v_mov_b32_e32 v181, s25
	v_pk_add_f32 v[180:181], s[18:19], v[180:181]
	s_add_i32 s24, s0, s1
	v_add_f32_e32 v136, v180, v181
	v_fmamk_f32 v136, v136, 0x3a000000, v203
	v_mul_f32_e32 v140, 0x4f800000, v136
	v_cmp_gt_f32_e32 vcc, s37, v136
	v_mov_b32_e32 v180, v131
	v_mov_b32_e32 v181, v133
	v_cndmask_b32_e32 v136, v136, v140, vcc
	v_sqrt_f32_e32 v140, v136
	s_add_i32 s26, s24, -8
	s_ashr_i32 s27, s26, 31
	s_lshl_b64 s[28:29], s[26:27], 11
	v_add_u32_e32 v131, -1, v140
	v_fma_f32 v165, -v131, v140, v136
	v_cmp_ge_f32_e64 s[18:19], 0, v165
	v_add_u32_e32 v165, 1, v140
	s_nop 0
	v_cndmask_b32_e64 v131, v140, v131, s[18:19]
	v_fma_f32 v140, -v165, v140, v136
	v_cmp_lt_f32_e64 s[18:19], 0, v140
	s_nop 1
	v_cndmask_b32_e64 v131, v131, v165, s[18:19]
	v_mul_f32_e32 v140, 0x37800000, v131
	v_cndmask_b32_e32 v131, v131, v140, vcc
	v_cmp_class_f32_e32 vcc, v136, v204
	s_nop 1
	v_cndmask_b32_e32 v131, v131, v136, vcc
	v_div_scale_f32 v136, s[18:19], v131, v131, 1.0
	v_rcp_f32_e32 v140, v136
	s_lshl_b64 s[18:19], s[26:27], 12
	v_fma_f32 v130, -v136, v140, 1.0
	v_fmac_f32_e32 v140, v130, v140
	v_div_scale_f32 v130, vcc, 1.0, v131, 1.0
	v_mul_f32_e32 v132, v130, v140
	v_fma_f32 v133, -v136, v132, v130
	v_fmac_f32_e32 v132, v133, v140
	v_fma_f32 v130, -v136, v132, v130
	v_div_fmas_f32 v130, v130, v140, v132
	v_div_fixup_f32 v140, v130, v131, 1.0
	ds_read_b128 v[130:133], v196
	ds_read_b128 v[210:213], v197
	v_pk_mul_f32 v[226:227], v[172:173], v[140:141] op_sel_hi:[1,0]
	v_pk_mul_f32 v[172:173], v[176:177], v[140:141] op_sel_hi:[1,0]
	ds_read_b128 v[214:217], v197 offset:1024
	ds_read_b128 v[218:221], v196 offset:1024
	v_pk_mul_f32 v[174:175], v[192:193], v[140:141] op_sel_hi:[1,0]
	s_waitcnt lgkmcnt(2)
	v_pk_fma_f32 v[176:177], v[130:131], v[226:227], v[210:211]
	v_pk_fma_f32 v[172:173], v[132:133], v[172:173], v[212:213]
	v_bfe_u32 v130, v176, 16, 1
	v_add3_u32 v130, v176, v130, s38
	v_bfe_u32 v131, v177, 16, 1
	v_lshrrev_b32_e32 v130, 16, v130
	v_add3_u32 v131, v177, v131, s38
	v_and_or_b32 v165, v131, s31, v130
	v_bfe_u32 v130, v172, 16, 1
	v_add3_u32 v130, v172, v130, s38
	v_bfe_u32 v131, v173, 16, 1
	v_lshrrev_b32_e32 v130, 16, v130
	v_add3_u32 v131, v173, v131, s38
	v_pk_mul_f32 v[132:133], v[222:223], v[140:141] op_sel_hi:[1,0]
	v_and_or_b32 v234, v131, s31, v130
	v_pk_mul_f32 v[130:131], v[180:181], v[140:141] op_sel_hi:[1,0]
	s_waitcnt lgkmcnt(0)
	v_pk_fma_f32 v[132:133], v[218:219], v[132:133], v[214:215]
	v_pk_fma_f32 v[130:131], v[220:221], v[130:131], v[216:217]
	v_bfe_u32 v136, v132, 16, 1
	v_mov_b32_e32 v180, v132
	v_mov_b32_e32 v181, v176
	v_mov_b32_e32 v210, v133
	v_mov_b32_e32 v211, v177
	v_add3_u32 v136, v132, v136, s38
	v_bfe_u32 v168, v133, 16, 1
	v_pk_add_f32 v[180:181], v[180:181], v[210:211]
	v_mov_b32_e32 v210, v131
	v_mov_b32_e32 v211, v173
	v_mov_b32_e32 v212, v130
	v_mov_b32_e32 v213, v172
	v_lshrrev_b32_e32 v136, 16, v136
	v_add3_u32 v168, v133, v168, s38
	v_pk_add_f32 v[210:211], v[210:211], v[212:213]
	v_and_or_b32 v235, v168, s31, v136
	v_bfe_u32 v136, v130, 16, 1
	v_pk_add_f32 v[180:181], v[180:181], v[210:211]
	ds_read_b128 v[210:213], v197 offset:2048
	ds_read_b128 v[214:217], v196 offset:2048
	v_add3_u32 v136, v130, v136, s38
	v_bfe_u32 v168, v131, 16, 1
	v_lshrrev_b32_e32 v136, 16, v136
	v_add3_u32 v168, v131, v168, s38
	v_and_or_b32 v236, v168, s31, v136
	v_add_f32_e32 v136, 0, v181
	v_add_f32_e32 v227, v180, v136
	v_pk_mul_f32 v[180:181], v[178:179], v[140:141] op_sel_hi:[1,0]
	v_pk_mul_f32 v[178:179], v[224:225], v[140:141] op_sel_hi:[1,0]
	s_waitcnt lgkmcnt(0)
; #define LAS __attribute__((address_space(3)))
; __device__ __forceinline__ unsigned pk2(float lo, float hi) { return f2bf(lo) | (f2bf(hi) << 16); }
; __device__ __forceinline__ void phase5(Frame& F, const Args& a) {
;     ...
;             for (int j = 0; j < 8; ++j) { if ((j & 3) == 0) asm volatile("" ::: "memory"); const f32x4 gg = *((const LAS f32x4*)prm + lane + 64 * j), bb = *((const LAS f32x4*)(prm + D) + lane + 64 * j);
;                 v[j] = v[j] * rstd * gg + bb; xw8[j].x = pk2(v[j].x, v[j].y); xw8[j].y = pk2(v[j].z, v[j].w); s += (v[j].x + v[j].y) + (v[j].z + v[j].w); }
;             store_row_b8<8, 512>((unsigned char*)(X1 + (size_t)m * D), lane, xw8);
	v_pk_fma_f32 v[180:181], v[214:215], v[180:181], v[210:211]
	ds_read_b128 v[218:221], v197 offset:3072
	ds_read_b128 v[222:225], v196 offset:3072
	v_bfe_u32 v136, v180, 16, 1
	v_pk_fma_f32 v[178:179], v[216:217], v[178:179], v[212:213]
	v_add3_u32 v136, v180, v136, s38
	v_bfe_u32 v168, v181, 16, 1
	v_lshrrev_b32_e32 v136, 16, v136
	v_add3_u32 v168, v181, v168, s38
	v_mov_b32_e32 v210, v180
	v_mov_b32_e32 v211, v179
	v_pk_mov_b32 v[212:213], v[180:181], v[178:179] op_sel:[1,0]
	v_and_or_b32 v237, v168, s31, v136
	v_bfe_u32 v136, v178, 16, 1
	v_pk_add_f32 v[210:211], v[210:211], v[212:213]
	v_add3_u32 v136, v178, v136, s38
	v_bfe_u32 v168, v179, 16, 1
	v_pk_add_f32 v[228:229], v[210:211], v[210:211] op_sel_hi:[0,1]
	v_pk_mul_f32 v[210:211], v[134:135], v[140:141] op_sel_hi:[1,0]
	v_lshrrev_b32_e32 v136, 16, v136
	v_add3_u32 v168, v179, v168, s38
	v_pk_mul_f32 v[134:135], v[166:167], v[140:141] op_sel_hi:[1,0]
	s_waitcnt lgkmcnt(0)
	v_pk_fma_f32 v[166:167], v[210:211], v[222:223], v[218:219]
	ds_read_b128 v[210:213], v196 offset:4096
	ds_read_b128 v[214:217], v197 offset:4096
	v_and_or_b32 v238, v168, s31, v136
	v_bfe_u32 v136, v166, 16, 1
	v_add3_u32 v136, v166, v136, s38
	v_bfe_u32 v168, v167, 16, 1
	v_pk_fma_f32 v[134:135], v[134:135], v[224:225], v[220:221]
	v_lshrrev_b32_e32 v136, 16, v136
	v_add3_u32 v168, v167, v168, s38
	v_and_or_b32 v239, v168, s31, v136
	v_bfe_u32 v136, v134, 16, 1
	v_pk_mul_f32 v[184:185], v[184:185], v[140:141] op_sel_hi:[1,0]
	v_add3_u32 v136, v134, v136, s38
	v_bfe_u32 v168, v135, 16, 1
	ds_read_b128 v[218:221], v197 offset:5120
	ds_read_b128 v[222:225], v196 offset:5120
	s_waitcnt lgkmcnt(2)
	v_pk_fma_f32 v[184:185], v[184:185], v[212:213], v[216:217]
	v_pk_fma_f32 v[188:189], v[174:175], v[210:211], v[214:215]
	v_lshrrev_b32_e32 v136, 16, v136
	v_add3_u32 v168, v135, v168, s38
	v_add_f32_e32 v231, v166, v167
	v_add_f32_e32 v233, v135, v134
	v_mov_b32_e32 v230, v188
	v_mov_b32_e32 v232, v189
	v_mov_b32_e32 v228, v185
	v_mov_b32_e32 v226, v184
	v_and_or_b32 v240, v168, s31, v136
	v_bfe_u32 v136, v188, 16, 1
	v_pk_add_f32 v[174:175], v[230:231], v[232:233]
	v_pk_add_f32 v[192:193], v[228:229], v[226:227]
	v_add3_u32 v136, v188, v136, s38
	v_bfe_u32 v168, v189, 16, 1
	v_pk_add_f32 v[174:175], v[174:175], v[192:193]
	v_lshrrev_b32_e32 v136, 16, v136
	v_add3_u32 v168, v189, v168, s38
	v_pk_add_f32 v[226:227], v[174:175], v[174:175] op_sel:[0,1] op_sel_hi:[1,0]
	v_pk_mul_f32 v[174:175], v[170:171], v[140:141] op_sel_hi:[1,0]
	v_pk_mul_f32 v[170:171], v[194:195], v[140:141] op_sel_hi:[1,0]
	v_and_or_b32 v241, v168, s31, v136
	v_bfe_u32 v136, v184, 16, 1
	s_waitcnt lgkmcnt(0)
	v_pk_fma_f32 v[170:171], v[170:171], v[224:225], v[220:221]
	v_pk_fma_f32 v[174:175], v[174:175], v[222:223], v[218:219]
	v_add3_u32 v136, v184, v136, s38
	v_bfe_u32 v168, v185, 16, 1
	v_mov_b32_e32 v192, v174
	v_mov_b32_e32 v193, v171
	v_pk_mov_b32 v[194:195], v[174:175], v[170:171] op_sel:[1,0]
	v_lshrrev_b32_e32 v136, 16, v136
	v_add3_u32 v168, v185, v168, s38
	v_pk_add_f32 v[192:193], v[192:193], v[194:195]
	v_and_or_b32 v242, v168, s31, v136
	v_bfe_u32 v136, v174, 16, 1
	v_pk_add_f32 v[222:223], v[192:193], v[192:193] op_sel:[0,1] op_sel_hi:[1,0]
	ds_read_b128 v[192:195], v197 offset:6144
	ds_read_b128 v[210:213], v196 offset:6144
	v_add3_u32 v136, v174, v136, s38
	v_bfe_u32 v168, v175, 16, 1
	v_lshrrev_b32_e32 v136, 16, v136
	v_add3_u32 v168, v175, v168, s38
	v_and_or_b32 v228, v168, s31, v136
	v_bfe_u32 v136, v170, 16, 1
	v_add3_u32 v136, v170, v136, s38
	v_bfe_u32 v168, v171, 16, 1
	v_pk_mul_f32 v[224:225], v[182:183], v[140:141] op_sel_hi:[1,0]
	v_lshrrev_b32_e32 v136, 16, v136
	v_add3_u32 v168, v171, v168, s38
	v_pk_mul_f32 v[182:183], v[186:187], v[140:141] op_sel_hi:[1,0]
	s_waitcnt lgkmcnt(0)
	v_pk_fma_f32 v[186:187], v[224:225], v[210:211], v[192:193]
	v_and_or_b32 v229, v168, s31, v136
	v_bfe_u32 v136, v186, 16, 1
	ds_read_b128 v[214:217], v197 offset:7168
	ds_read_b128 v[218:221], v196 offset:7168
	v_add3_u32 v136, v186, v136, s38
	v_bfe_u32 v168, v187, 16, 1
	v_pk_fma_f32 v[182:183], v[182:183], v[212:213], v[194:195]
	v_lshrrev_b32_e32 v136, 16, v136
	v_add3_u32 v168, v187, v168, s38
	v_and_or_b32 v224, v168, s31, v136
	v_bfe_u32 v136, v182, 16, 1
	v_add3_u32 v136, v182, v136, s38
	v_bfe_u32 v168, v183, 16, 1
	v_lshrrev_b32_e32 v136, 16, v136
	v_add3_u32 v168, v183, v168, s38
	v_pk_mul_f32 v[190:191], v[190:191], v[140:141] op_sel_hi:[1,0]
	v_and_or_b32 v225, v168, s31, v136
	v_mov_b32_e32 v136, v169
	s_waitcnt lgkmcnt(0)
; __device__ __forceinline__ int dpp_x1(int v) { return __builtin_amdgcn_mov_dpp(v, 0xB1, 0xF, 0xF, true); }
; template <int NP, int STEP> __device__ __forceinline__ void store_row_b8(unsigned char* row, int lane, const v2u (&w)[NP]) {
;     const int odd = lane & 1; unsigned char* base = row + (lane >> 1) * 16;
; #pragma unroll
;     for (int i = 0; i < NP / 2; ++i) { const v2u A = w[2 * i], B = w[2 * i + 1];
;         const unsigned r0 = (unsigned)dpp_x1((int)(odd ? A.x : B.x)), r1 = (unsigned)dpp_x1((int)(odd ? A.y : B.y));
;         v4u o; o.x = odd ? r0 : A.x; o.y = odd ? r1 : A.y; o.z = odd ? B.x : r0; o.w = odd ? B.y : r1;
;         *(v4u*)(base + STEP * (2 * i + odd)) = o; }
; }
; __device__ __forceinline__ void phase5(Frame& F, const Args& a) {
;     ...
;             store_row_b8<8, 512>((unsigned char*)(X1 + (size_t)m * D), lane, xw8);
;             mean = wave_sum(s) * (1.f / D); s2 = 0.f;
; #pragma unroll
;             for (int j = 0; j < 8; ++j) { v[j] = v[j] - mean; s2 += (v[j].x * v[j].x + v[j].y * v[j].y) + (v[j].z * v[j].z + v[j].w * v[j].w); }
	v_pk_fma_f32 v[168:169], v[190:191], v[218:219], v[214:215]
	v_pk_mul_f32 v[136:137], v[136:137], v[140:141] op_sel_hi:[1,0]
	v_bfe_u32 v140, v168, 16, 1
	v_add3_u32 v140, v168, v140, s38
	v_bfe_u32 v190, v169, 16, 1
	v_pk_fma_f32 v[136:137], v[136:137], v[220:221], v[216:217]
	v_lshrrev_b32_e32 v140, 16, v140
	v_add3_u32 v190, v169, v190, s38
	v_and_or_b32 v214, v190, s31, v140
	v_bfe_u32 v140, v136, 16, 1
	v_add3_u32 v140, v136, v140, s38
	v_bfe_u32 v190, v137, 16, 1
	v_add_f32_e32 v192, v186, v187
	v_add_f32_e32 v194, v183, v182
	v_lshrrev_b32_e32 v140, 16, v140
	v_add3_u32 v190, v137, v190, s38
	v_mov_b32_e32 v227, v168
	v_mov_b32_e32 v223, v169
	v_mov_b32_e32 v193, v137
	v_mov_b32_e32 v195, v136
	v_and_or_b32 v215, v190, s31, v140
	v_pk_add_f32 v[190:191], v[226:227], v[222:223]
	v_pk_add_f32 v[192:193], v[192:193], v[194:195]
	v_lshl_add_u64 v[194:195], v[158:159], 0, s[18:19]
	v_pk_add_f32 v[190:191], v[190:191], v[192:193]
	v_cndmask_b32_e64 v216, v225, v215, s[4:5]
	v_add_f32_e32 v140, v190, v191
	v_cndmask_b32_e64 v190, v165, v235, s[4:5]
	s_nop 0
	v_add_f32_dpp v140, v140, v140 quad_perm:[1,0,3,2] row_mask:0xf bank_mask:0xf bound_ctrl:1
	v_mov_b32_dpp v192, v190 quad_perm:[1,0,3,2] row_mask:0xf bank_mask:0xf bound_ctrl:1
	v_cndmask_b32_e64 v190, v234, v236, s[4:5]
	v_add_f32_dpp v140, v140, v140 quad_perm:[2,3,0,1] row_mask:0xf bank_mask:0xf bound_ctrl:1
	s_nop 0
	v_mov_b32_dpp v193, v190 quad_perm:[1,0,3,2] row_mask:0xf bank_mask:0xf bound_ctrl:1
	v_cndmask_b32_e64 v190, v192, v165, s[4:5]
	v_cndmask_b32_e64 v191, v193, v234, s[4:5]
	v_cndmask_b32_e64 v192, v235, v192, s[4:5]
	v_cndmask_b32_e64 v193, v236, v193, s[4:5]
	global_store_dwordx4 v[194:195], v[190:193], off
	v_cndmask_b32_e64 v165, v237, v239, s[4:5]
	v_add_f32_dpp v140, v140, v140 row_half_mirror row_mask:0xf bank_mask:0xf bound_ctrl:1
	v_cndmask_b32_e64 v190, v238, v240, s[4:5]
	v_mov_b32_dpp v165, v165 quad_perm:[1,0,3,2] row_mask:0xf bank_mask:0xf bound_ctrl:1
	v_cndmask_b32_e64 v192, v239, v165, s[4:5]
	v_mov_b32_dpp v193, v190 quad_perm:[1,0,3,2] row_mask:0xf bank_mask:0xf bound_ctrl:1
	v_cndmask_b32_e64 v190, v165, v237, s[4:5]
	v_cndmask_b32_e64 v191, v193, v238, s[4:5]
	v_cndmask_b32_e64 v193, v240, v193, s[4:5]
	global_store_dwordx4 v[194:195], v[190:193], off offset:1024
	v_cndmask_b32_e64 v165, v241, v228, s[4:5]
	v_add_f32_dpp v140, v140, v140 row_mirror row_mask:0xf bank_mask:0xf bound_ctrl:1
	v_cndmask_b32_e64 v190, v242, v229, s[4:5]
	v_mov_b32_dpp v165, v165 quad_perm:[1,0,3,2] row_mask:0xf bank_mask:0xf bound_ctrl:1
	v_cndmask_b32_e64 v192, v228, v165, s[4:5]
	v_mov_b32_dpp v193, v190 quad_perm:[1,0,3,2] row_mask:0xf bank_mask:0xf bound_ctrl:1
	v_cndmask_b32_e64 v190, v165, v241, s[4:5]
	v_cndmask_b32_e64 v191, v193, v242, s[4:5]
	v_cndmask_b32_e64 v193, v229, v193, s[4:5]
	v_readlane_b32 s25, v140, 16
	v_readlane_b32 s44, v140, 48
	global_store_dwordx4 v[194:195], v[190:193], off offset:2048
	v_readlane_b32 s18, v140, 0
	v_readlane_b32 s19, v140, 32
	v_mov_b32_e32 v190, s25
	v_mov_b32_e32 v191, s44
	v_pk_add_f32 v[190:191], s[18:19], v[190:191]
	v_cndmask_b32_e64 v165, v224, v214, s[4:5]
	v_add_f32_e32 v217, v190, v191
	v_fmamk_f32 v177, v217, 0xba000000, v177
	v_fmamk_f32 v133, v217, 0xba000000, v133
	v_fmamk_f32 v173, v217, 0xba000000, v173
	v_fmac_f32_e32 v176, 0xba000000, v217
	v_fmamk_f32 v131, v217, 0xba000000, v131
	v_fmac_f32_e32 v132, 0xba000000, v217
	v_mov_b32_e32 v192, v177
	v_mov_b32_e32 v193, v133
	v_fmac_f32_e32 v172, 0xba000000, v217
	v_fmac_f32_e32 v130, 0xba000000, v217
	v_mov_b32_e32 v190, v176
	v_mov_b32_e32 v191, v132
	v_pk_mul_f32 v[192:193], v[192:193], v[192:193]
	v_mov_b32_e32 v210, v173
	v_mov_b32_e32 v211, v131
	v_pk_fma_f32 v[190:191], v[190:191], v[190:191], v[192:193]
	v_mov_b32_e32 v192, v172
	v_mov_b32_e32 v193, v130
	v_pk_mul_f32 v[210:211], v[210:211], v[210:211]
	v_fmamk_f32 v181, v217, 0xba000000, v181
	v_pk_fma_f32 v[192:193], v[192:193], v[192:193], v[210:211]
	v_fmac_f32_e32 v180, 0xba000000, v217
	v_fmamk_f32 v179, v217, 0xba000000, v179
	v_fmac_f32_e32 v178, 0xba000000, v217
	v_pk_add_f32 v[190:191], v[190:191], v[192:193]
	v_pk_mul_f32 v[192:193], v[178:179], v[178:179]
	v_pk_mul_f32 v[210:211], v[180:181], v[180:181]
	v_fmac_f32_e32 v166, 0xba000000, v217
	v_pk_mov_b32 v[212:213], v[210:211], v[192:193] op_sel:[1,0]
	v_mov_b32_e32 v211, v193
	v_fmamk_f32 v167, v217, 0xba000000, v167
	v_fmac_f32_e32 v134, 0xba000000, v217
	v_mul_f32_e32 v140, v166, v166
	v_pk_add_f32 v[192:193], v[212:213], v[210:211]
	v_fmamk_f32 v135, v217, 0xba000000, v135
	v_pk_fma_f32 v[210:211], v[166:167], v[166:167], v[140:141] op_sel_hi:[1,1,0]
	v_mul_f32_e32 v140, v134, v134
	v_pk_add_f32 v[190:191], v[190:191], v[190:191] op_sel_hi:[0,1]
	v_pk_add_f32 v[192:193], v[192:193], v[192:193] op_sel_hi:[0,1]
	v_pk_fma_f32 v[212:213], v[134:135], v[134:135], v[140:141] op_sel_hi:[1,1,0]
	v_fmamk_f32 v185, v217, 0xba000000, v185
	v_fmac_f32_e32 v184, 0xba000000, v217
	v_fmamk_f32 v189, v217, 0xba000000, v189
	v_fmac_f32_e32 v188, 0xba000000, v217
	v_mul_f32_e32 v210, v188, v188
	v_mul_f32_e32 v212, v189, v189
	v_mul_f32_e32 v192, v184, v184
	v_mul_f32_e32 v190, v185, v185
	v_pk_add_f32 v[210:211], v[210:211], v[212:213]
	v_pk_add_f32 v[190:191], v[192:193], v[190:191]
	v_fmamk_f32 v175, v217, 0xba000000, v175
	v_fmac_f32_e32 v174, 0xba000000, v217
	v_fmamk_f32 v171, v217, 0xba000000, v171
	v_fmac_f32_e32 v170, 0xba000000, v217
	v_pk_add_f32 v[190:191], v[210:211], v[190:191]
	v_pk_mul_f32 v[192:193], v[170:171], v[170:171]
	v_pk_mul_f32 v[210:211], v[174:175], v[174:175]
	v_fmac_f32_e32 v186, 0xba000000, v217
; __device__ __forceinline__ unsigned cvt_pk_bf16(float lo, float hi) { unsigned r; asm volatile("v_cvt_pk_bf16_f32 %0, %1, %2" : "=v"(r) : "v"(lo), "v"(hi)); return r; }
; #define LAS __attribute__((address_space(3)))
; __device__ __forceinline__ void phase5(Frame& F, const Args& a) {
;     ...
;             for (int j = 0; j < 8; ++j) { v[j] = v[j] - mean; s2 += (v[j].x * v[j].x + v[j].y * v[j].y) + (v[j].z * v[j].z + v[j].w * v[j].w); }
;             rstd = 1.f / sqrtf(wave_sum(s2) * (1.f / D) + LN_EPS);
;             unsigned* o4 = (unsigned*)(H8 + (size_t)m * D) + lane; float am = 0.f;
; #pragma unroll
;             for (int j = 0; j < 8; ++j) { if ((j & 3) == 0) asm volatile("" ::: "memory"); const f32x4 sh = *((const LAS f32x4*)(prm + 2 * D) + lane + 64 * j), sc1 = *((const LAS f32x4*)(prm + 3 * D) + lane + 64 * j);
;                 v[j] = v[j] * rstd * sc1 + sh; am = fmaxf(fmaxf(am, fmaxf(fabsf(v[j].x), fabsf(v[j].y))), fmaxf(fabsf(v[j].z), fabsf(v[j].w)));
;                 { const unsigned h0 = pg8::cvt_pk_bf16(v[j].x, v[j].y), h1 = pg8::cvt_pk_bf16(v[j].z, v[j].w);
;                   v2u hv; hv.x = h0; hv.y = h1; v2u lv; lv.x = pg8::cvt_pk_bf16(v[j].x - bflo(h0), v[j].y - bfhi(h0)); lv.y = pg8::cvt_pk_bf16(v[j].z - bflo(h1), v[j].w - bfhi(h1));
;                   *((LAS v2u*)(hsh + wid * HSB) + lane + 64 * j) = hv; *((LAS v2u*)(hsl + wid * HSB) + lane + 64 * j) = lv; } }
	v_pk_mov_b32 v[212:213], v[210:211], v[192:193] op_sel:[1,0]
	v_mov_b32_e32 v211, v193
	v_fmamk_f32 v187, v217, 0xba000000, v187
	v_fmac_f32_e32 v182, 0xba000000, v217
	v_mul_f32_e32 v140, v186, v186
	v_pk_add_f32 v[192:193], v[212:213], v[210:211]
	v_fmamk_f32 v183, v217, 0xba000000, v183
	v_pk_fma_f32 v[210:211], v[186:187], v[186:187], v[140:141] op_sel_hi:[1,1,0]
	v_mul_f32_e32 v140, v182, v182
	v_pk_add_f32 v[190:191], v[190:191], v[190:191] op_sel_hi:[0,1]
	v_pk_add_f32 v[192:193], v[192:193], v[192:193] op_sel_hi:[0,1]
	v_pk_fma_f32 v[212:213], v[182:183], v[182:183], v[140:141] op_sel_hi:[1,1,0]
	v_fmamk_f32 v137, v217, 0xba000000, v137
	v_fmac_f32_e32 v136, 0xba000000, v217
	v_fmamk_f32 v169, v217, 0xba000000, v169
	v_fmac_f32_e32 v168, 0xba000000, v217
	v_mul_f32_e32 v210, v168, v168
	v_mul_f32_e32 v212, v169, v169
	v_mul_f32_e32 v192, v136, v136
	v_mul_f32_e32 v190, v137, v137
	v_pk_add_f32 v[210:211], v[210:211], v[212:213]
	v_pk_add_f32 v[190:191], v[192:193], v[190:191]
	v_mov_b32_dpp v193, v216 quad_perm:[1,0,3,2] row_mask:0xf bank_mask:0xf bound_ctrl:1
	v_pk_add_f32 v[190:191], v[210:211], v[190:191]
	v_mov_b32_dpp v165, v165 quad_perm:[1,0,3,2] row_mask:0xf bank_mask:0xf bound_ctrl:1
	v_add_f32_e32 v140, v190, v191
	s_nop 1
	v_add_f32_dpp v140, v140, v140 quad_perm:[1,0,3,2] row_mask:0xf bank_mask:0xf bound_ctrl:1
	s_nop 1
	v_add_f32_dpp v140, v140, v140 quad_perm:[2,3,0,1] row_mask:0xf bank_mask:0xf bound_ctrl:1
	s_nop 1
	v_add_f32_dpp v140, v140, v140 row_half_mirror row_mask:0xf bank_mask:0xf bound_ctrl:1
	s_nop 1
	v_add_f32_dpp v140, v140, v140 row_mirror row_mask:0xf bank_mask:0xf bound_ctrl:1
	s_nop 0
	v_readlane_b32 s25, v140, 16
	v_readlane_b32 s44, v140, 48
	v_readlane_b32 s18, v140, 0
	v_readlane_b32 s19, v140, 32
	v_mov_b32_e32 v190, s25
	v_mov_b32_e32 v191, s44
	v_pk_add_f32 v[190:191], s[18:19], v[190:191]
	s_nop 0
	v_add_f32_e32 v140, v190, v191
	v_fmamk_f32 v140, v140, 0x3a000000, v203
	v_mul_f32_e32 v190, 0x4f800000, v140
	v_cmp_gt_f32_e32 vcc, s37, v140
	v_cndmask_b32_e64 v191, v193, v225, s[4:5]
	v_cndmask_b32_e64 v193, v215, v193, s[4:5]
	v_cndmask_b32_e32 v140, v140, v190, vcc
	v_sqrt_f32_e32 v192, v140
	v_cndmask_b32_e64 v190, v165, v224, s[4:5]
	v_add_u32_e32 v210, -1, v192
	v_fma_f32 v211, -v210, v192, v140
	v_cmp_ge_f32_e64 s[18:19], 0, v211
	v_add_u32_e32 v211, 1, v192
	s_nop 0
	v_cndmask_b32_e64 v210, v192, v210, s[18:19]
	v_fma_f32 v192, -v211, v192, v140
	v_cmp_lt_f32_e64 s[18:19], 0, v192
	s_nop 1
	v_cndmask_b32_e64 v192, v210, v211, s[18:19]
	v_mul_f32_e32 v210, 0x37800000, v192
	v_cndmask_b32_e32 v192, v192, v210, vcc
	v_cmp_class_f32_e32 vcc, v140, v204
	s_nop 1
	v_cndmask_b32_e32 v140, v192, v140, vcc
	v_div_scale_f32 v210, s[18:19], v140, v140, 1.0
	v_rcp_f32_e32 v216, v210
	v_cndmask_b32_e64 v192, v214, v165, s[4:5]
	global_store_dwordx4 v[194:195], v[190:193], off offset:3072
	v_fma_f32 v165, -v210, v216, 1.0
	v_fmac_f32_e32 v216, v165, v216
	v_div_scale_f32 v165, vcc, 1.0, v140, 1.0
	v_mul_f32_e32 v194, v165, v216
	v_fma_f32 v190, -v210, v194, v165
	v_fmac_f32_e32 v194, v190, v216
	v_fma_f32 v165, -v210, v194, v165
	ds_read_b128 v[190:193], v198
	ds_read_b128 v[210:213], v199
	v_div_fmas_f32 v165, v165, v216, v194
	v_div_fixup_f32 v140, v165, v140, 1.0
	v_pk_mul_f32 v[176:177], v[176:177], v[140:141] op_sel_hi:[1,0]
	v_pk_mul_f32 v[172:173], v[172:173], v[140:141] op_sel_hi:[1,0]
	s_waitcnt lgkmcnt(0)
	v_pk_fma_f32 v[176:177], v[210:211], v[176:177], v[190:191]
	v_pk_fma_f32 v[172:173], v[212:213], v[172:173], v[192:193]
	v_cvt_pk_bf16_f32 v190, v176, v177
	v_pk_mul_f32 v[132:133], v[132:133], v[140:141] op_sel_hi:[1,0]
	v_lshlrev_b32_e32 v192, 16, v190
	v_and_b32_e32 v193, 0xffff0000, v190
	v_sub_f32_e32 v192, v176, v192
	v_sub_f32_e32 v193, v177, v193
	v_cvt_pk_bf16_f32 v191, v172, v173
	v_cvt_pk_bf16_f32 v192, v192, v193
	v_pk_mul_f32 v[130:131], v[130:131], v[140:141] op_sel_hi:[1,0]
	v_lshlrev_b32_e32 v193, 16, v191
	v_sub_f32_e32 v193, v172, v193
	v_and_b32_e32 v194, 0xffff0000, v191
	v_sub_f32_e32 v194, v173, v194
	v_cvt_pk_bf16_f32 v193, v193, v194
	ds_write_b64 v200, v[190:191]
	ds_write_b64 v200, v[192:193] offset:32896
	ds_read_b128 v[190:193], v199 offset:1024
	ds_read_b128 v[210:213], v198 offset:1024
	v_pk_mul_f32 v[180:181], v[180:181], v[140:141] op_sel_hi:[1,0]
	v_pk_mul_f32 v[178:179], v[178:179], v[140:141] op_sel_hi:[1,0]
	v_max_f32_e64 v165, |v176|, |v177|
	v_max_f32_e64 v194, |v172|, |v173|
	s_waitcnt lgkmcnt(0)
	v_pk_fma_f32 v[130:131], v[130:131], v[192:193], v[212:213]
	v_pk_fma_f32 v[132:133], v[132:133], v[190:191], v[210:211]
	v_max3_f32 v165, v165, 0, v194
	v_cvt_pk_bf16_f32 v190, v132, v133
	v_cvt_pk_bf16_f32 v191, v130, v131
	v_max_f32_e64 v194, |v132|, |v133|
	v_lshlrev_b32_e32 v192, 16, v190
	v_and_b32_e32 v193, 0xffff0000, v190
	v_sub_f32_e32 v192, v132, v192
	v_sub_f32_e32 v193, v133, v193
	v_cvt_pk_bf16_f32 v192, v192, v193
	v_lshlrev_b32_e32 v193, 16, v191
	v_sub_f32_e32 v193, v130, v193
	v_and_b32_e32 v195, 0xffff0000, v191
	v_sub_f32_e32 v195, v131, v195
	v_cvt_pk_bf16_f32 v193, v193, v195
	ds_write_b64 v200, v[190:191] offset:512
	ds_write_b64 v200, v[192:193] offset:33408
	ds_read_b128 v[190:193], v199 offset:2048
	ds_read_b128 v[210:213], v198 offset:2048
	v_max_f32_e64 v195, |v130|, |v131|
	v_max3_f32 v165, v165, v194, v195
	v_pk_mul_f32 v[166:167], v[166:167], v[140:141] op_sel_hi:[1,0]
	v_pk_mul_f32 v[134:135], v[134:135], v[140:141] op_sel_hi:[1,0]
	s_waitcnt lgkmcnt(0)
; __device__ __forceinline__ unsigned cvt_pk_bf16(float lo, float hi) { unsigned r; asm volatile("v_cvt_pk_bf16_f32 %0, %1, %2" : "=v"(r) : "v"(lo), "v"(hi)); return r; }
; #define LAS __attribute__((address_space(3)))
; __device__ __forceinline__ void phase5(Frame& F, const Args& a) {
;     ...
;             for (int j = 0; j < 8; ++j) { if ((j & 3) == 0) asm volatile("" ::: "memory"); const f32x4 sh = *((const LAS f32x4*)(prm + 2 * D) + lane + 64 * j), sc1 = *((const LAS f32x4*)(prm + 3 * D) + lane + 64 * j);
;                 v[j] = v[j] * rstd * sc1 + sh; am = fmaxf(fmaxf(am, fmaxf(fabsf(v[j].x), fabsf(v[j].y))), fmaxf(fabsf(v[j].z), fabsf(v[j].w)));
;                 { const unsigned h0 = pg8::cvt_pk_bf16(v[j].x, v[j].y), h1 = pg8::cvt_pk_bf16(v[j].z, v[j].w);
;                   v2u hv; hv.x = h0; hv.y = h1; v2u lv; lv.x = pg8::cvt_pk_bf16(v[j].x - bflo(h0), v[j].y - bfhi(h0)); lv.y = pg8::cvt_pk_bf16(v[j].z - bflo(h1), v[j].w - bfhi(h1));
;                   *((LAS v2u*)(hsh + wid * HSB) + lane + 64 * j) = hv; *((LAS v2u*)(hsl + wid * HSB) + lane + 64 * j) = lv; } }
	v_pk_fma_f32 v[178:179], v[178:179], v[192:193], v[212:213]
	v_pk_fma_f32 v[180:181], v[180:181], v[190:191], v[210:211]
	v_pk_mul_f32 v[188:189], v[188:189], v[140:141] op_sel_hi:[1,0]
	v_cvt_pk_bf16_f32 v190, v180, v181
	v_cvt_pk_bf16_f32 v191, v178, v179
	v_max_f32_e64 v194, |v180|, |v181|
	v_lshlrev_b32_e32 v192, 16, v190
	v_and_b32_e32 v193, 0xffff0000, v190
	v_sub_f32_e32 v192, v180, v192
	v_sub_f32_e32 v193, v181, v193
	v_cvt_pk_bf16_f32 v192, v192, v193
	v_lshlrev_b32_e32 v193, 16, v191
	v_sub_f32_e32 v193, v178, v193
	v_and_b32_e32 v195, 0xffff0000, v191
	v_sub_f32_e32 v195, v179, v195
	v_cvt_pk_bf16_f32 v193, v193, v195
	ds_write_b64 v200, v[190:191] offset:1024
	ds_write_b64 v200, v[192:193] offset:33920
	ds_read_b128 v[190:193], v199 offset:3072
	ds_read_b128 v[210:213], v198 offset:3072
	v_max_f32_e64 v195, |v178|, |v179|
	v_max3_f32 v165, v165, v194, v195
	v_pk_mul_f32 v[184:185], v[184:185], v[140:141] op_sel_hi:[1,0]
	v_pk_mul_f32 v[174:175], v[174:175], v[140:141] op_sel_hi:[1,0]
	s_waitcnt lgkmcnt(0)
	v_pk_fma_f32 v[134:135], v[134:135], v[192:193], v[212:213]
	v_pk_fma_f32 v[166:167], v[166:167], v[190:191], v[210:211]
	v_pk_mul_f32 v[170:171], v[170:171], v[140:141] op_sel_hi:[1,0]
	v_cvt_pk_bf16_f32 v190, v166, v167
	v_cvt_pk_bf16_f32 v191, v134, v135
	v_max_f32_e64 v194, |v166|, |v167|
	v_lshlrev_b32_e32 v192, 16, v190
	v_and_b32_e32 v193, 0xffff0000, v190
	v_sub_f32_e32 v192, v166, v192
	v_sub_f32_e32 v193, v167, v193
	v_cvt_pk_bf16_f32 v192, v192, v193
	v_lshlrev_b32_e32 v193, 16, v191
	v_sub_f32_e32 v193, v134, v193
	v_and_b32_e32 v195, 0xffff0000, v191
	v_sub_f32_e32 v195, v135, v195
	v_cvt_pk_bf16_f32 v193, v193, v195
	ds_write_b64 v200, v[190:191] offset:1536
	ds_write_b64 v200, v[192:193] offset:34432
	ds_read_b128 v[190:193], v198 offset:4096
	ds_read_b128 v[210:213], v199 offset:4096
	v_max_f32_e64 v195, |v134|, |v135|
	v_max3_f32 v165, v165, v194, v195
	v_pk_mul_f32 v[182:183], v[182:183], v[140:141] op_sel_hi:[1,0]
	v_pk_mul_f32 v[168:169], v[168:169], v[140:141] op_sel_hi:[1,0]
	s_waitcnt lgkmcnt(0)
	v_pk_fma_f32 v[212:213], v[184:185], v[212:213], v[192:193]
	v_pk_fma_f32 v[210:211], v[188:189], v[210:211], v[190:191]
	v_pk_mul_f32 v[136:137], v[136:137], v[140:141] op_sel_hi:[1,0]
	v_cvt_pk_bf16_f32 v184, v210, v211
	v_cvt_pk_bf16_f32 v185, v212, v213
	v_max_f32_e64 v214, |v210|, |v211|
	v_lshlrev_b32_e32 v188, 16, v184
	v_and_b32_e32 v189, 0xffff0000, v184
	v_sub_f32_e32 v188, v210, v188
	v_sub_f32_e32 v189, v211, v189
	v_cvt_pk_bf16_f32 v188, v188, v189
	v_lshlrev_b32_e32 v189, 16, v185
	v_sub_f32_e32 v189, v212, v189
	v_and_b32_e32 v190, 0xffff0000, v185
	v_sub_f32_e32 v190, v213, v190
	v_cvt_pk_bf16_f32 v189, v189, v190
	ds_write_b64 v200, v[184:185] offset:2048
	ds_write_b64 v200, v[188:189] offset:34944
	ds_read_b128 v[188:191], v199 offset:5120
	ds_read_b128 v[192:195], v198 offset:5120
	v_max_f32_e64 v184, |v212|, |v213|
	v_max3_f32 v165, v165, v214, v184
	s_waitcnt lgkmcnt(0)
	v_pk_fma_f32 v[174:175], v[174:175], v[188:189], v[192:193]
	s_nop 0
	v_cvt_pk_bf16_f32 v184, v174, v175
	v_pk_fma_f32 v[170:171], v[170:171], v[190:191], v[194:195]
	v_lshlrev_b32_e32 v188, 16, v184
	v_and_b32_e32 v189, 0xffff0000, v184
	v_sub_f32_e32 v188, v174, v188
	v_sub_f32_e32 v189, v175, v189
	v_cvt_pk_bf16_f32 v185, v170, v171
	v_cvt_pk_bf16_f32 v188, v188, v189
	v_max_f32_e64 v214, |v174|, |v175|
	v_lshlrev_b32_e32 v189, 16, v185
	v_sub_f32_e32 v189, v170, v189
	v_and_b32_e32 v190, 0xffff0000, v185
	v_sub_f32_e32 v190, v171, v190
	v_cvt_pk_bf16_f32 v189, v189, v190
	ds_write_b64 v200, v[184:185] offset:2560
	ds_write_b64 v200, v[188:189] offset:35456
	ds_read_b128 v[188:191], v199 offset:6144
	ds_read_b128 v[192:195], v198 offset:6144
	v_max_f32_e64 v184, |v170|, |v171|
	v_max3_f32 v165, v165, v214, v184
	v_pk_mul_f32 v[184:185], v[186:187], v[140:141] op_sel_hi:[1,0]
	s_waitcnt lgkmcnt(0)
	v_pk_fma_f32 v[190:191], v[182:183], v[190:191], v[194:195]
	v_pk_fma_f32 v[192:193], v[184:185], v[188:189], v[192:193]
	v_max_f32_e64 v195, |v190|, |v191|
	v_cvt_pk_bf16_f32 v182, v192, v193
	v_cvt_pk_bf16_f32 v183, v190, v191
	v_max_f32_e64 v194, |v192|, |v193|
	v_lshlrev_b32_e32 v184, 16, v182
	v_and_b32_e32 v185, 0xffff0000, v182
	v_sub_f32_e32 v184, v192, v184
	v_sub_f32_e32 v185, v193, v185
	v_cvt_pk_bf16_f32 v184, v184, v185
	v_lshlrev_b32_e32 v185, 16, v183
	v_sub_f32_e32 v185, v190, v185
	v_and_b32_e32 v186, 0xffff0000, v183
	v_sub_f32_e32 v186, v191, v186
	v_cvt_pk_bf16_f32 v185, v185, v186
	ds_write_b64 v200, v[182:183] offset:3072
	ds_write_b64 v200, v[184:185] offset:35968
	ds_read_b128 v[182:185], v199 offset:7168
	ds_read_b128 v[186:189], v198 offset:7168
	v_max3_f32 v165, v165, v194, v195
	s_waitcnt lgkmcnt(0)
; __device__ __forceinline__ unsigned q8x4(float a, float b, float c, float d, float sc) {
;     const float M = 12582912.0f;
;     const unsigned ua = __builtin_bit_cast(unsigned, __builtin_amdgcn_fmed3f(__builtin_fmaf(a, sc, M), M - 127.0f, M + 127.0f)), ub = __builtin_bit_cast(unsigned, __builtin_amdgcn_fmed3f(__builtin_fmaf(b, sc, M), M - 127.0f, M + 127.0f));
;     const unsigned uc = __builtin_bit_cast(unsigned, __builtin_amdgcn_fmed3f(__builtin_fmaf(c, sc, M), M - 127.0f, M + 127.0f)), ud = __builtin_bit_cast(unsigned, __builtin_amdgcn_fmed3f(__builtin_fmaf(d, sc, M), M - 127.0f, M + 127.0f));
;     return __builtin_amdgcn_perm(ub, ua, 0x0c0c0400u) | __builtin_amdgcn_perm(ud, uc, 0x04000c0cu);
; }
; __device__ __forceinline__ void phase5(Frame& F, const Args& a) {
;     ...
;             am = fmaxf(wave_max(am), 1e-20f);
;             const float qs = 127.0f / am;
;             { unsigned hw[8];
; #pragma unroll
;               for (int j = 0; j < 8; ++j) hw[j] = q8x4(v[j].x, v[j].y, v[j].z, v[j].w, qs);
	v_pk_fma_f32 v[184:185], v[136:137], v[184:185], v[188:189]
	v_pk_fma_f32 v[168:169], v[168:169], v[182:183], v[186:187]
	v_max_f32_e64 v137, |v184|, |v185|
	v_max_f32_e64 v136, |v168|, |v169|
	v_max3_f32 v136, v165, v136, v137
	v_cvt_pk_bf16_f32 v182, v168, v169
	v_cvt_pk_bf16_f32 v183, v184, v185
	s_nop 0
	v_lshlrev_b32_e32 v137, 16, v182
	v_mov_b32_dpp v165, v136 quad_perm:[1,0,3,2] row_mask:0xf bank_mask:0xf bound_ctrl:1
	v_max_f32_e32 v165, v165, v165
	v_max_f32_e32 v136, v136, v165
	v_sub_f32_e32 v137, v168, v137
	v_and_b32_e32 v140, 0xffff0000, v182
	v_mov_b32_dpp v165, v136 quad_perm:[2,3,0,1] row_mask:0xf bank_mask:0xf bound_ctrl:1
	v_max_f32_e32 v165, v165, v165
	v_max_f32_e32 v136, v136, v165
	v_sub_f32_e32 v140, v169, v140
	v_cvt_pk_bf16_f32 v186, v137, v140
	v_lshlrev_b32_e32 v137, 16, v183
	v_mov_b32_dpp v165, v136 row_half_mirror row_mask:0xf bank_mask:0xf bound_ctrl:1
	v_max_f32_e32 v165, v165, v165
	v_max_f32_e32 v136, v136, v165
	v_sub_f32_e32 v137, v184, v137
	v_and_b32_e32 v140, 0xffff0000, v183
	v_mov_b32_dpp v165, v136 row_mirror row_mask:0xf bank_mask:0xf bound_ctrl:1
	v_max_f32_e32 v165, v165, v165
	v_max_f32_e32 v136, v136, v165
	v_sub_f32_e32 v140, v185, v140
	v_readlane_b32 s18, v136, 0
	v_readlane_b32 s19, v136, 16
	s_nop 0
	v_max_f32_e64 v187, s18, s18
	v_max_f32_e64 v165, s19, s19
	v_readlane_b32 s18, v136, 32
	v_readlane_b32 s19, v136, 48
	v_max_f32_e32 v165, v187, v165
	v_max_f32_e64 v187, s18, s18
	v_max_f32_e64 v136, s19, s19
	v_max_f32_e32 v136, v187, v136
	v_max3_f32 v136, v165, v136, s39
	v_div_scale_f32 v165, s[18:19], v136, v136, s40
	v_rcp_f32_e32 v188, v165
	v_cvt_pk_bf16_f32 v187, v137, v140
	ds_write_b64 v200, v[182:183] offset:3584
	ds_write_b64 v200, v[186:187] offset:36480
	v_fma_f32 v137, -v165, v188, 1.0
	v_fmac_f32_e32 v188, v137, v188
	v_div_scale_f32 v137, vcc, s40, v136, s40
	v_mul_f32_e32 v140, v137, v188
	v_fma_f32 v182, -v165, v140, v137
	v_fmac_f32_e32 v140, v182, v188
	v_fma_f32 v137, -v165, v140, v137
	v_div_fmas_f32 v137, v137, v188, v140
	v_div_fixup_f32 v137, v137, v136, s40
	v_fmaak_f32 v140, v176, v137, 0x4b400000
	v_fmaak_f32 v165, v177, v137, 0x4b400000
	v_fmaak_f32 v172, v172, v137, 0x4b400000
	v_fmaak_f32 v173, v173, v137, 0x4b400000
	v_fmaak_f32 v132, v132, v137, 0x4b400000
	v_fmaak_f32 v133, v133, v137, 0x4b400000
	v_fmaak_f32 v130, v130, v137, 0x4b400000
	v_fmaak_f32 v131, v131, v137, 0x4b400000
	v_med3_f32 v140, v140, s41, v208
	v_med3_f32 v165, v165, s41, v208
	v_med3_f32 v172, v172, s41, v208
	v_med3_f32 v173, v173, s41, v208
	v_med3_f32 v132, v132, s41, v208
	v_med3_f32 v133, v133, s41, v208
	v_med3_f32 v130, v130, s41, v208
	v_med3_f32 v131, v131, s41, v208
	v_perm_b32 v140, v165, v140, s42
	v_perm_b32 v165, v173, v172, s43
	v_perm_b32 v132, v133, v132, s42
	v_perm_b32 v130, v131, v130, s43
	v_or_b32_e32 v140, v140, v165
	v_or_b32_e32 v130, v132, v130
	v_fmaak_f32 v131, v180, v137, 0x4b400000
	v_fmaak_f32 v132, v181, v137, 0x4b400000
	v_fmaak_f32 v133, v178, v137, 0x4b400000
	v_fmaak_f32 v165, v179, v137, 0x4b400000
	v_med3_f32 v131, v131, s41, v208
	v_med3_f32 v132, v132, s41, v208
	v_med3_f32 v133, v133, s41, v208
	v_med3_f32 v165, v165, s41, v208
	v_perm_b32 v131, v132, v131, s42
	v_perm_b32 v132, v165, v133, s43
	v_or_b32_e32 v131, v131, v132
	v_fmaak_f32 v132, v166, v137, 0x4b400000
	v_fmaak_f32 v133, v167, v137, 0x4b400000
	v_fmaak_f32 v134, v134, v137, 0x4b400000
	v_fmaak_f32 v135, v135, v137, 0x4b400000
	v_med3_f32 v132, v132, s41, v208
	v_med3_f32 v133, v133, s41, v208
	v_med3_f32 v134, v134, s41, v208
	v_med3_f32 v135, v135, s41, v208
	v_perm_b32 v132, v133, v132, s42
	v_perm_b32 v133, v135, v134, s43
	v_or_b32_e32 v132, v132, v133
	v_fmaak_f32 v133, v210, v137, 0x4b400000
	v_fmaak_f32 v134, v211, v137, 0x4b400000
; __device__ __forceinline__ int dpp_x1(int v) { return __builtin_amdgcn_mov_dpp(v, 0xB1, 0xF, 0xF, true); }
; __device__ __forceinline__ int dpp_x2(int v) { return __builtin_amdgcn_mov_dpp(v, 0x4E, 0xF, 0xF, true); }
; __device__ __forceinline__ void quad_transpose(int (&v)[4], int p) {
;     const bool lo2 = p < 2, ev = (p & 1) == 0;
; #pragma unroll
;     for (int i = 0; i < 2; ++i) { int t = lo2 ? v[i + 2] : v[i]; t = dpp_x2(t); if (lo2) v[i + 2] = t; else v[i] = t; }
; #pragma unroll
;     for (int i = 0; i < 4; i += 2) { int t = ev ? v[i + 1] : v[i]; t = dpp_x1(t); if (ev) v[i + 1] = t; else v[i] = t; }
; }
; __device__ __forceinline__ void store_row_b4(unsigned char* row, int lane, const unsigned (&w)[8]) {
;     const int p = lane & 3; unsigned char* base = row + (lane >> 2) * 16;
; #pragma unroll
;     for (int g = 0; g < 2; ++g) { int v[4] = {(int)w[4 * g], (int)w[4 * g + 1], (int)w[4 * g + 2], (int)w[4 * g + 3]}; quad_transpose(v, p);
;         v4u o; o.x = (unsigned)v[0]; o.y = (unsigned)v[1]; o.z = (unsigned)v[2]; o.w = (unsigned)v[3]; *(v4u*)(base + 256 * (4 * g + p)) = o; }
; }
; __device__ __forceinline__ void phase5(Frame& F, const Args& a) {
;     ...
;             { unsigned hw[8];
; #pragma unroll
;               for (int j = 0; j < 8; ++j) hw[j] = q8x4(v[j].x, v[j].y, v[j].z, v[j].w, qs);
;               store_row_b4(H8 + (size_t)m * D, lane, hw); }
;             if (lane == 0) ((float*)(a.ws + WS_RSH2))[m] = am * (1.0f / 127.0f);
	v_fmaak_f32 v135, v212, v137, 0x4b400000
	v_fmaak_f32 v165, v213, v137, 0x4b400000
	v_med3_f32 v133, v133, s41, v208
	v_med3_f32 v134, v134, s41, v208
	v_med3_f32 v135, v135, s41, v208
	v_med3_f32 v165, v165, s41, v208
	v_perm_b32 v133, v134, v133, s42
	v_perm_b32 v134, v165, v135, s43
	v_or_b32_e32 v165, v133, v134
	v_fmaak_f32 v133, v174, v137, 0x4b400000
	v_fmaak_f32 v134, v175, v137, 0x4b400000
	v_fmaak_f32 v135, v170, v137, 0x4b400000
	v_fmaak_f32 v166, v171, v137, 0x4b400000
	v_med3_f32 v133, v133, s41, v208
	v_med3_f32 v134, v134, s41, v208
	v_med3_f32 v135, v135, s41, v208
	v_med3_f32 v166, v166, s41, v208
	v_perm_b32 v133, v134, v133, s42
	v_perm_b32 v134, v166, v135, s43
	v_or_b32_e32 v166, v133, v134
	v_fmaak_f32 v133, v192, v137, 0x4b400000
	v_fmaak_f32 v134, v193, v137, 0x4b400000
	v_fmaak_f32 v135, v190, v137, 0x4b400000
	v_fmaak_f32 v167, v191, v137, 0x4b400000
	v_med3_f32 v133, v133, s41, v208
	v_med3_f32 v134, v134, s41, v208
	v_med3_f32 v135, v135, s41, v208
	v_med3_f32 v167, v167, s41, v208
	v_perm_b32 v133, v134, v133, s42
	v_perm_b32 v134, v167, v135, s43
	v_or_b32_e32 v167, v133, v134
	v_fmaak_f32 v133, v168, v137, 0x4b400000
	v_fmaak_f32 v134, v169, v137, 0x4b400000
	v_fmaak_f32 v135, v184, v137, 0x4b400000
	v_fmaak_f32 v137, v185, v137, 0x4b400000
	v_med3_f32 v133, v133, s41, v208
	v_med3_f32 v134, v134, s41, v208
	v_med3_f32 v135, v135, s41, v208
	v_med3_f32 v137, v137, s41, v208
	v_perm_b32 v133, v134, v133, s42
	v_perm_b32 v134, v137, v135, s43
	v_or_b32_e32 v137, v133, v134
	v_cndmask_b32_e64 v133, v140, v131, s[6:7]
	s_nop 1
	v_mov_b32_dpp v133, v133 quad_perm:[2,3,0,1] row_mask:0xf bank_mask:0xf bound_ctrl:1
	v_cndmask_b32_e64 v134, v131, v133, s[6:7]
	v_cndmask_b32_e64 v131, v130, v132, s[6:7]
	v_cndmask_b32_e64 v133, v133, v140, s[6:7]
	s_nop 0
	v_mov_b32_dpp v131, v131 quad_perm:[2,3,0,1] row_mask:0xf bank_mask:0xf bound_ctrl:1
	v_cndmask_b32_e64 v130, v131, v130, s[6:7]
	v_cndmask_b32_e64 v132, v132, v131, s[6:7]
	v_cndmask_b32_e64 v131, v133, v130, s[4:5]
	s_nop 1
	v_mov_b32_dpp v135, v131 quad_perm:[1,0,3,2] row_mask:0xf bank_mask:0xf bound_ctrl:1
	v_cndmask_b32_e64 v131, v130, v135, s[4:5]
	v_cndmask_b32_e64 v130, v135, v133, s[4:5]
	v_cndmask_b32_e64 v133, v134, v132, s[4:5]
	s_nop 1
	v_mov_b32_dpp v135, v133 quad_perm:[1,0,3,2] row_mask:0xf bank_mask:0xf bound_ctrl:1
	v_cndmask_b32_e64 v133, v132, v135, s[4:5]
	v_cndmask_b32_e64 v132, v135, v134, s[4:5]
	v_lshl_add_u64 v[134:135], v[160:161], 0, s[28:29]
	global_store_dwordx4 v[134:135], v[130:133], off
	s_nop 1
	v_cndmask_b32_e64 v130, v165, v167, s[6:7]
	v_cndmask_b32_e64 v131, v166, v137, s[6:7]
	s_nop 0
	v_mov_b32_dpp v130, v130 quad_perm:[2,3,0,1] row_mask:0xf bank_mask:0xf bound_ctrl:1
	v_mov_b32_dpp v131, v131 quad_perm:[2,3,0,1] row_mask:0xf bank_mask:0xf bound_ctrl:1
	v_cndmask_b32_e64 v132, v167, v130, s[6:7]
	v_cndmask_b32_e64 v130, v130, v165, s[6:7]
	v_cndmask_b32_e64 v133, v137, v131, s[6:7]
	v_cndmask_b32_e64 v131, v131, v166, s[6:7]
	v_cndmask_b32_e64 v137, v130, v131, s[4:5]
	s_nop 1
	v_mov_b32_dpp v137, v137 quad_perm:[1,0,3,2] row_mask:0xf bank_mask:0xf bound_ctrl:1
	v_cndmask_b32_e64 v131, v131, v137, s[4:5]
	v_cndmask_b32_e64 v130, v137, v130, s[4:5]
	v_cndmask_b32_e64 v137, v132, v133, s[4:5]
	s_nop 1
	v_mov_b32_dpp v137, v137 quad_perm:[1,0,3,2] row_mask:0xf bank_mask:0xf bound_ctrl:1
	v_cndmask_b32_e64 v133, v133, v137, s[4:5]
	v_cndmask_b32_e64 v132, v137, v132, s[4:5]
	global_store_dwordx4 v[134:135], v[130:133], off offset:1024
	s_and_saveexec_b64 s[18:19], s[8:9]
	s_cbranch_execz .LBB0_629
	s_lshl_b64 s[26:27], s[26:27], 2
	s_add_u32 s26, s35, s26
	s_addc_u32 s27, s36, s27
	v_mul_f32_e32 v130, 0x3c010204, v136
	global_store_dword v141, v130, s[26:27]

; #define LDS_WAIT() asm volatile("s_waitcnt lgkmcnt(0)" ::: "memory")
; __device__ __forceinline__ void phase5(Frame& F, const Args& a) {
;     ...
;         if (sb + 8 < rows_per_wg) {
; #pragma unroll
;             for (int j = 0; j < 8; ++j) ynx[j] = *((const v2u*)(Y1 + (size_t)(m + 8) * D) + lane + 64 * j);
;         }
;         LDS_WAIT();
;         P5_BAR();
;         {
;             float lv = rbv;
; #pragma unroll
;             for (int k = 0; k < 8; ++k) lv += part[(k * 8 + wid) * 32 + (lane & 31)];
;             float tv[4]; int ti[4];
; #pragma unroll
;             for (int k = 0; k < 4; ++k) {
;                 float v = lv;
;                 v = fmaxf(v, __builtin_bit_cast(float, __builtin_amdgcn_mov_dpp(__builtin_bit_cast(int, v), 0xB1, 0xF, 0xF, true)));
;                 v = fmaxf(v, __builtin_bit_cast(float, __builtin_amdgcn_mov_dpp(__builtin_bit_cast(int, v), 0x4E, 0xF, 0xF, true)));
;                 v = fmaxf(v, __builtin_bit_cast(float, __builtin_amdgcn_mov_dpp(__builtin_bit_cast(int, v), 0x141, 0xF, 0xF, true)));
;                 v = fmaxf(v, __builtin_bit_cast(float, __builtin_amdgcn_mov_dpp(__builtin_bit_cast(int, v), 0x140, 0xF, 0xF, true)));
;                 const float best = fmaxf(__builtin_bit_cast(float, __builtin_amdgcn_readlane(__builtin_bit_cast(int, v), 0)), __builtin_bit_cast(float, __builtin_amdgcn_readlane(__builtin_bit_cast(int, v), 16)));
;                 const unsigned long long bal = __builtin_amdgcn_ballot_w64(lv == best);
;                 const int bi = (int)__builtin_ctzll(bal) & 31;
;                 tv[k] = best; ti[k] = bi;
;                 lv = ((lane & 31) == bi) ? -3.0e38f : lv; }
;             const float e1 = __expf(tv[1] - tv[0]), e2 = __expf(tv[2] - tv[0]), e3 = __expf(tv[3] - tv[0]), inv = 1.0f / (1.0f + e1 + e2 + e3);
;             if (lane < 4) {
;                 const int k = lane; const int e = k == 0 ? ti[0] : k == 1 ? ti[1] : k == 2 ? ti[2] : ti[3];
;                 const float gt = (k == 0 ? 1.0f : k == 1 ? e1 : k == 2 ? e2 : e3) * inv;
;                 TOPI[m * 4 + k] = e; GATE[m * 4 + k] = gt;
;                 const int lr = __hip_atomic_fetch_add(&hist[e], 1, __ATOMIC_RELAXED, __HIP_MEMORY_SCOPE_WORKGROUP);
;                 const int idx = (li * NWAVES + wid) * 4 + k;
;                 asg_e[idx] = e; asg_r[idx] = lr; asg_m[idx] = m * 4 + k;
;             }
.LBB0_631:
	s_or_b64 exec, exec, s[18:19]
	s_cmp_ge_i32 s1, s30
	s_cselect_b64 s[26:27], -1, 0
	s_and_b64 vcc, exec, s[26:27]
	s_cbranch_vccnz .LBB0_633
.LBB0_633:
	s_waitcnt lgkmcnt(0)
	s_waitcnt lgkmcnt(0)
	s_barrier
	ds_read2st64_b32 v[130:131], v206 offset1:4
	ds_read2st64_b32 v[132:133], v206 offset0:8 offset1:12
	ds_read2st64_b32 v[134:135], v206 offset0:16 offset1:20
	ds_read2st64_b32 v[136:137], v206 offset0:24 offset1:28
	s_waitcnt lgkmcnt(3)
	v_add_f32_e32 v130, v139, v130
	v_add_f32_e32 v130, v130, v131
	s_waitcnt lgkmcnt(2)
	v_add_f32_e32 v130, v130, v132
	v_add_f32_e32 v130, v130, v133
	s_waitcnt lgkmcnt(1)
	v_add_f32_e32 v130, v130, v134
	v_add_f32_e32 v130, v130, v135
	s_waitcnt lgkmcnt(0)
	v_add_f32_e32 v130, v130, v136
	v_add_f32_e32 v131, v130, v137
	s_nop 1
	v_mov_b32_dpp v130, v131 quad_perm:[1,0,3,2] row_mask:0xf bank_mask:0xf bound_ctrl:1
	v_max_f32_e32 v130, v130, v130
	v_max_f32_e32 v130, v131, v130
	s_nop 1
	v_mov_b32_dpp v132, v130 quad_perm:[2,3,0,1] row_mask:0xf bank_mask:0xf bound_ctrl:1
	v_max_f32_e32 v132, v132, v132
	v_max_f32_e32 v130, v130, v132
	s_nop 1
	v_mov_b32_dpp v132, v130 row_half_mirror row_mask:0xf bank_mask:0xf bound_ctrl:1
	v_max_f32_e32 v132, v132, v132
	v_max_f32_e32 v130, v130, v132
	s_nop 1
	v_mov_b32_dpp v132, v130 row_mirror row_mask:0xf bank_mask:0xf bound_ctrl:1
	v_max_f32_e32 v132, v132, v132
	v_max_f32_e32 v130, v130, v132
	s_nop 0
	v_readlane_b32 s18, v130, 0
	v_readlane_b32 s19, v130, 16
	s_nop 0
	v_max_f32_e64 v132, s18, s18
	v_max_f32_e64 v130, s19, s19
	v_max_f32_e32 v130, v132, v130
	v_cmp_eq_f32_e32 vcc, v131, v130
	s_ff1_i32_b64 s18, vcc
	s_and_b32 s28, s18, 31
	v_cmp_ne_u32_e32 vcc, s28, v1
	s_nop 1
	v_cndmask_b32_e32 v132, v209, v131, vcc
	s_nop 1
	v_mov_b32_dpp v131, v132 quad_perm:[1,0,3,2] row_mask:0xf bank_mask:0xf bound_ctrl:1
	v_max_f32_e32 v131, v131, v131
	v_max_f32_e32 v131, v132, v131
	s_nop 1
	v_mov_b32_dpp v133, v131 quad_perm:[2,3,0,1] row_mask:0xf bank_mask:0xf bound_ctrl:1
	v_max_f32_e32 v133, v133, v133
	v_max_f32_e32 v131, v131, v133
	s_nop 1
	v_mov_b32_dpp v133, v131 row_half_mirror row_mask:0xf bank_mask:0xf bound_ctrl:1
	v_max_f32_e32 v133, v133, v133
	v_max_f32_e32 v131, v131, v133
	s_nop 1
	v_mov_b32_dpp v133, v131 row_mirror row_mask:0xf bank_mask:0xf bound_ctrl:1
	v_max_f32_e32 v133, v133, v133
	v_max_f32_e32 v131, v131, v133
	s_nop 0
	v_readlane_b32 s18, v131, 0
	v_readlane_b32 s19, v131, 16
	s_nop 0
	v_max_f32_e64 v133, s18, s18
	v_max_f32_e64 v131, s19, s19
	v_max_f32_e32 v131, v133, v131
	v_cmp_eq_f32_e32 vcc, v132, v131
	s_ff1_i32_b64 s18, vcc
	s_and_b32 s29, s18, 31
	v_cmp_ne_u32_e32 vcc, s29, v1
	s_nop 1
	v_cndmask_b32_e32 v133, v209, v132, vcc
	s_nop 1
	v_mov_b32_dpp v132, v133 quad_perm:[1,0,3,2] row_mask:0xf bank_mask:0xf bound_ctrl:1
	v_max_f32_e32 v132, v132, v132
	v_max_f32_e32 v132, v133, v132
	s_nop 1
	v_mov_b32_dpp v134, v132 quad_perm:[2,3,0,1] row_mask:0xf bank_mask:0xf bound_ctrl:1
	v_max_f32_e32 v134, v134, v134
	v_max_f32_e32 v132, v132, v134
	s_nop 1
	v_mov_b32_dpp v134, v132 row_half_mirror row_mask:0xf bank_mask:0xf bound_ctrl:1
	v_max_f32_e32 v134, v134, v134
	v_max_f32_e32 v132, v132, v134
	s_nop 1
	v_mov_b32_dpp v134, v132 row_mirror row_mask:0xf bank_mask:0xf bound_ctrl:1
	v_max_f32_e32 v134, v134, v134
	v_max_f32_e32 v132, v132, v134
	s_nop 0
	v_readlane_b32 s18, v132, 0
	v_readlane_b32 s19, v132, 16
	s_nop 0
	v_max_f32_e64 v134, s18, s18
	v_max_f32_e64 v132, s19, s19
	v_max_f32_e32 v132, v134, v132
	v_cmp_eq_f32_e32 vcc, v133, v132
	s_ff1_i32_b64 s18, vcc
	s_and_b32 s44, s18, 31
	v_cmp_ne_u32_e32 vcc, s44, v1
	s_nop 1
	v_cndmask_b32_e32 v134, v209, v133, vcc
	s_nop 1
	v_mov_b32_dpp v133, v134 quad_perm:[1,0,3,2] row_mask:0xf bank_mask:0xf bound_ctrl:1
	v_max_f32_e32 v133, v133, v133
	v_max_f32_e32 v133, v134, v133
	s_nop 1
	v_mov_b32_dpp v135, v133 quad_perm:[2,3,0,1] row_mask:0xf bank_mask:0xf bound_ctrl:1
	v_max_f32_e32 v135, v135, v135
	v_max_f32_e32 v133, v133, v135
	s_nop 1
	v_mov_b32_dpp v135, v133 row_half_mirror row_mask:0xf bank_mask:0xf bound_ctrl:1
	v_max_f32_e32 v135, v135, v135
	v_max_f32_e32 v133, v133, v135
	s_nop 1
	v_mov_b32_dpp v135, v133 row_mirror row_mask:0xf bank_mask:0xf bound_ctrl:1
	v_max_f32_e32 v135, v135, v135
	v_max_f32_e32 v133, v133, v135
	s_nop 0
	v_readlane_b32 s18, v133, 0
	v_readlane_b32 s19, v133, 16
	s_nop 0
	v_max_f32_e64 v135, s18, s18
	v_max_f32_e64 v133, s19, s19
	v_max_f32_e32 v133, v135, v133
	v_cmp_eq_f32_e64 s[18:19], v134, v133
	s_and_saveexec_b64 s[24:25], s[12:13]
	s_cbranch_execz .LBB0_626
	v_sub_f32_e32 v131, v131, v130
	v_mul_f32_e32 v131, 0x3fb8aa3b, v131
	v_sub_f32_e32 v132, v132, v130
	v_exp_f32_e32 v131, v131
	v_mul_f32_e32 v132, 0x3fb8aa3b, v132
	v_sub_f32_e32 v130, v133, v130
	v_exp_f32_e32 v132, v132
	v_mul_f32_e32 v130, 0x3fb8aa3b, v130
	v_exp_f32_e32 v130, v130
	v_add_f32_e32 v133, 1.0, v131
	v_add_f32_e32 v133, v133, v132
	s_ff1_i32_b64 s18, s[18:19]
	v_add_f32_e32 v133, v133, v130
	v_div_scale_f32 v134, s[46:47], v133, v133, 1.0
	v_rcp_f32_e32 v135, v134
	s_and_b32 s18, s18, 31
	v_cndmask_b32_e64 v130, v130, v132, s[16:17]
	v_cndmask_b32_e64 v130, v130, v131, s[14:15]
	v_fma_f32 v136, -v134, v135, 1.0
	v_fmac_f32_e32 v135, v136, v135
	v_div_scale_f32 v136, vcc, 1.0, v133, 1.0
	v_mul_f32_e32 v137, v136, v135
	v_fma_f32 v140, -v134, v137, v136
	v_fmac_f32_e32 v137, v140, v135
	v_fma_f32 v134, -v134, v137, v136
	v_div_fmas_f32 v134, v134, v135, v137
	v_div_fixup_f32 v133, v134, v133, 1.0
	v_mov_b32_e32 v134, s18
	v_mov_b32_e32 v135, s44
	v_cndmask_b32_e64 v134, v134, v135, s[16:17]
	v_mov_b32_e32 v135, s29
	v_cndmask_b32_e64 v134, v134, v135, s[14:15]
	v_mov_b32_e32 v135, s28
	v_cndmask_b32_e64 v130, v130, 1.0, s[8:9]
	v_ashrrev_i32_e32 v165, 31, v164
	v_cndmask_b32_e64 v134, v134, v135, s[8:9]
	v_mul_f32_e32 v135, v133, v130
	v_lshlrev_b64 v[130:131], 2, v[164:165]
	v_lshl_add_u64 v[132:133], s[20:21], 0, v[130:131]
	v_lshl_add_u64 v[130:131], s[22:23], 0, v[130:131]
	global_store_dword v[130:131], v135, off
	v_lshl_add_u32 v130, v134, 2, 0
	global_store_dword v[132:133], v134, off
	v_add_u32_e32 v130, 0x16000, v130
	ds_add_rtn_u32 v130, v130, v207
	v_add_u32_e32 v131, 0xffffe000, v202
	ds_write_b32 v131, v134
	v_add_u32_e32 v131, 0xfffff000, v202
	s_waitcnt lgkmcnt(1)
	ds_write_b32 v131, v130
	ds_write_b32 v202, v164
	s_branch .LBB0_626
